# P11 streaming dwordx4 loads carry the nt cache hint (stores unchanged); otherwise identical to v86
# speedup vs baseline: 1.0007x; 1.0007x over previous
.LBB0_1337:
	v_mbcnt_lo_u32_b32 v0, -1, 0
	s_add_u32 s13, s92, 0x28ee1c00
	v_mbcnt_hi_u32_b32 v0, -1, v0
	s_addc_u32 s14, s93, 0
	v_lshlrev_b32_e32 v1, 3, v0
	s_add_u32 s6, s92, 0xb661c00
	v_and_b32_e32 v16, 0x1f8, v1
	s_addc_u32 s7, s93, 0
	s_cmpk_gt_i32 s8, 0x1fff
	v_lshlrev_b32_e32 v207, 2, v16
	v_lshlrev_b32_e32 v18, 1, v16
	v_and_b32_e32 v206, 63, v0
	s_cbranch_scc1 .LBB0_1340
	s_add_u32 s0, s92, 0x28a000
	v_readlane_b32 s16, v253, 29
	s_waitcnt vmcnt(6)
	v_or_b32_e32 v20, 0x200, v16
	s_addc_u32 s1, s93, 0
	v_readlane_b32 s17, v253, 30
	v_lshlrev_b32_e32 v0, 2, v20
	v_or_b32_e32 v22, 0x400, v16
	global_load_dwordx4 v[34:37], v207, s[0:1] offset:16 nt
	global_load_dwordx4 v[30:33], v207, s[0:1] nt
	s_nop 0
	global_load_dwordx4 v[38:41], v207, s[16:17] offset:16 nt
	global_load_dwordx4 v[42:45], v207, s[16:17] nt
	global_load_dwordx4 v[46:49], v0, s[0:1] offset:16 nt
	global_load_dwordx4 v[50:53], v0, s[0:1] nt
	global_load_dwordx4 v[54:57], v207, s[16:17] offset:2064 nt
	global_load_dwordx4 v[58:61], v207, s[16:17] offset:2048 nt
	v_lshlrev_b32_e32 v0, 2, v22
	v_or_b32_e32 v24, 0x600, v16
	global_load_dwordx4 v[62:65], v0, s[0:1] offset:16 nt
	global_load_dwordx4 v[76:79], v0, s[0:1] nt
	global_load_dwordx4 v[82:85], v0, s[16:17] offset:16 nt
	global_load_dwordx4 v[86:89], v0, s[16:17] nt
	v_lshlrev_b32_e32 v0, 2, v24
	s_ashr_i32 s9, s8, 31
	global_load_dwordx4 v[96:99], v0, s[0:1] offset:16 nt
	global_load_dwordx4 v[102:105], v0, s[0:1] nt
	global_load_dwordx4 v[110:113], v0, s[16:17] offset:16 nt
	global_load_dwordx4 v[122:125], v0, s[16:17] nt
	s_lshl_b64 s[0:1], s[8:9], 12
	s_add_u32 s0, s6, s0
	s_addc_u32 s1, s7, s1
	global_load_dwordx4 v[0:3], v18, s[0:1] offset:3072 nt
	global_load_dwordx4 v[4:7], v18, s[0:1] offset:2048 nt
	global_load_dwordx4 v[8:11], v18, s[0:1] offset:1024 nt
	global_load_dwordx4 v[12:15], v18, s[0:1] nt
	s_lshl_b64 s[0:1], s[8:9], 13
	s_add_u32 s10, s13, s0
	s_addc_u32 s11, s14, s1
	s_add_u32 s16, s10, 0x1800
	v_readlane_b32 s18, v253, 31
	s_addc_u32 s17, s11, 0
	v_readlane_b32 s19, v253, 32
	s_add_u32 s18, s10, 0x1000
	s_addc_u32 s19, s11, 0
	global_load_dwordx2 v[142:143], v22, s[16:17]
	global_load_dwordx2 v[134:135], v20, s[16:17]
	s_nop 0
	global_load_dwordx2 v[108:109], v20, s[18:19]
	global_load_dwordx2 v[116:117], v22, s[18:19]
	global_load_dwordx2 v[94:95], v16, s[10:11] offset:3584
	global_load_dwordx2 v[90:91], v16, s[10:11] offset:3072
	global_load_dwordx2 v[80:81], v16, s[10:11] offset:2560
	global_load_dwordx2 v[72:73], v16, s[10:11] offset:2048
	global_load_dwordx2 v[66:67], v16, s[10:11] offset:1536
	global_load_dwordx2 v[68:69], v16, s[10:11] offset:1024
	global_load_dwordx2 v[70:71], v16, s[10:11] offset:512
	global_load_dwordx2 v[74:75], v16, s[10:11]
	global_load_dwordx2 v[190:191], v24, s[16:17]
	global_load_dwordx2 v[126:127], v16, s[16:17]
	global_load_dwordx2 v[120:121], v24, s[18:19]
	global_load_dwordx2 v[100:101], v16, s[18:19]
	v_mov_b32_e32 v17, 0
	s_add_u32 s0, s50, s0
	v_lshlrev_b32_e32 v92, 5, v206
	v_mov_b32_e32 v93, v17
	s_addc_u32 s1, s51, s1
	s_mov_b64 s[10:11], 0x1000
	v_mov_b32_e32 v19, v17
	s_ashr_i32 s3, s2, 31
	v_mov_b32_e32 v21, v17
	v_mov_b32_e32 v23, v17
	v_mov_b32_e32 v25, v17
	v_lshl_add_u64 v[26:27], s[6:7], 0, v[18:19]
	s_mov_b32 s12, 0x3d800000
	v_mov_b32_e32 v19, 0x358637bd
	v_readlane_b32 s20, v253, 33
	v_readlane_b32 s21, v253, 34
	v_readlane_b32 s22, v253, 35
	v_readlane_b32 s23, v253, 36
	v_readlane_b32 s24, v253, 37
	v_readlane_b32 s25, v253, 38
	v_readlane_b32 s26, v253, 39
	v_readlane_b32 s27, v253, 40
	v_readlane_b32 s28, v253, 41
	v_readlane_b32 s29, v253, 42
	v_readlane_b32 s30, v253, 43
	v_readlane_b32 s31, v253, 44
	s_waitcnt vmcnt(33)
	v_pk_mul_f32 v[34:35], v[34:35], v[38:39]
	s_waitcnt vmcnt(32)
	v_pk_mul_f32 v[28:29], v[32:33], v[44:45]
	v_pk_mul_f32 v[32:33], v[36:37], v[40:41]
	s_waitcnt vmcnt(28)
	v_pk_mul_f32 v[36:37], v[52:53], v[60:61]
	v_lshl_add_u64 v[60:61], s[0:1], 0, v[92:93]
	v_pk_mul_f32 v[30:31], v[30:31], v[42:43]
	v_pk_mul_f32 v[38:39], v[50:51], v[58:59]
	v_pk_mul_f32 v[40:41], v[48:49], v[56:57]
	v_pk_mul_f32 v[42:43], v[46:47], v[54:55]
	s_waitcnt vmcnt(24)
	v_pk_mul_f32 v[44:45], v[78:79], v[88:89]
	v_pk_mul_f32 v[46:47], v[76:77], v[86:87]
	v_pk_mul_f32 v[48:49], v[64:65], v[84:85]
	v_pk_mul_f32 v[50:51], v[62:63], v[82:83]
	s_waitcnt vmcnt(20)
	v_pk_mul_f32 v[52:53], v[104:105], v[124:125]
	v_pk_mul_f32 v[54:55], v[102:103], v[122:123]
	v_pk_mul_f32 v[56:57], v[98:99], v[112:113]
	v_pk_mul_f32 v[58:59], v[96:97], v[110:111]
	v_lshl_add_u64 v[60:61], v[60:61], 0, s[10:11]
	s_lshl_b64 s[10:11], s[2:3], 13
	s_mov_b32 s3, 0x800000
.LBB0_1339:
	s_add_i32 s1, s8, s2
	s_waitcnt vmcnt(4)
	v_cvt_pk_f32_fp8_e32 v[154:155], v74
	v_cvt_pk_f32_fp8_sdwa v[164:165], v70 src0_sel:WORD_1
	s_cmpk_lt_i32 s1, 0x2000
	v_cvt_pk_f32_fp8_sdwa v[156:157], v74 src0_sel:WORD_1
	v_cvt_pk_f32_fp8_e32 v[158:159], v75
	v_cvt_pk_f32_fp8_sdwa v[160:161], v75 src0_sel:WORD_1
	v_cvt_pk_f32_fp8_e32 v[162:163], v70
	v_cvt_pk_f32_fp8_e32 v[166:167], v71
	v_cvt_pk_f32_fp8_sdwa v[168:169], v71 src0_sel:WORD_1
	v_cvt_pk_f32_fp8_sdwa v[182:183], v69 src0_sel:WORD_1
	v_cvt_pk_f32_fp8_e32 v[184:185], v66
	v_cvt_pk_f32_fp8_sdwa v[194:195], v66 src0_sel:WORD_1
	v_cvt_pk_f32_fp8_e32 v[196:197], v67
	v_cvt_pk_f32_fp8_sdwa v[198:199], v67 src0_sel:WORD_1
	v_cvt_pk_f32_fp8_e32 v[66:67], v72
	v_cvt_pk_f32_fp8_sdwa v[76:77], v80 src0_sel:WORD_1
	s_cselect_b64 s[16:17], -1, 0
	v_cvt_pk_f32_fp8_e32 v[172:173], v68
	v_cvt_pk_f32_fp8_sdwa v[174:175], v68 src0_sel:WORD_1
	v_cvt_pk_f32_fp8_e32 v[180:181], v69
	v_cvt_pk_f32_fp8_sdwa v[68:69], v72 src0_sel:WORD_1
	v_cvt_pk_f32_fp8_e32 v[70:71], v73
	v_cvt_pk_f32_fp8_sdwa v[72:73], v73 src0_sel:WORD_1
	v_cvt_pk_f32_fp8_e32 v[74:75], v80
	v_cvt_pk_f32_fp8_e32 v[78:79], v81
	v_cvt_pk_f32_fp8_sdwa v[80:81], v81 src0_sel:WORD_1
	v_cvt_pk_f32_fp8_e32 v[84:85], v90
	v_cvt_pk_f32_fp8_sdwa v[86:87], v90 src0_sel:WORD_1
	v_cvt_pk_f32_fp8_e32 v[88:89], v91
	v_cvt_pk_f32_fp8_sdwa v[90:91], v91 src0_sel:WORD_1
	v_cvt_pk_f32_fp8_e32 v[92:93], v94
	v_cvt_pk_f32_fp8_sdwa v[148:149], v94 src0_sel:WORD_1
	v_cvt_pk_f32_fp8_e32 v[150:151], v95
	v_cvt_pk_f32_fp8_sdwa v[152:153], v95 src0_sel:WORD_1
	s_waitcnt vmcnt(0)
	v_cvt_pk_f32_fp8_e32 v[94:95], v100
	v_cvt_pk_f32_fp8_sdwa v[104:105], v108 src0_sel:WORD_1
	s_and_b64 vcc, s[16:17], exec
	v_cvt_pk_f32_fp8_sdwa v[96:97], v100 src0_sel:WORD_1
	v_cvt_pk_f32_fp8_e32 v[98:99], v101
	v_cvt_pk_f32_fp8_sdwa v[100:101], v101 src0_sel:WORD_1
	v_cvt_pk_f32_fp8_e32 v[102:103], v108
	v_cvt_pk_f32_fp8_e32 v[106:107], v109
	v_cvt_pk_f32_fp8_sdwa v[108:109], v109 src0_sel:WORD_1
	v_cvt_pk_f32_fp8_e32 v[110:111], v116
	v_cvt_pk_f32_fp8_sdwa v[112:113], v116 src0_sel:WORD_1
	v_cvt_pk_f32_fp8_e32 v[114:115], v117
	v_cvt_pk_f32_fp8_sdwa v[116:117], v117 src0_sel:WORD_1
	v_cvt_pk_f32_fp8_e32 v[118:119], v120
	v_cvt_pk_f32_fp8_sdwa v[170:171], v120 src0_sel:WORD_1
	v_cvt_pk_f32_fp8_e32 v[176:177], v121
	v_cvt_pk_f32_fp8_sdwa v[178:179], v121 src0_sel:WORD_1
	v_cvt_pk_f32_fp8_e32 v[120:121], v126
	v_cvt_pk_f32_fp8_sdwa v[130:131], v134 src0_sel:WORD_1
	s_cselect_b32 s0, s1, s8
	v_cvt_pk_f32_fp8_sdwa v[122:123], v126 src0_sel:WORD_1
	v_cvt_pk_f32_fp8_e32 v[124:125], v127
	v_cvt_pk_f32_fp8_sdwa v[126:127], v127 src0_sel:WORD_1
	v_cvt_pk_f32_fp8_e32 v[128:129], v134
	v_cvt_pk_f32_fp8_e32 v[132:133], v135
	v_cvt_pk_f32_fp8_sdwa v[134:135], v135 src0_sel:WORD_1
	v_cvt_pk_f32_fp8_e32 v[136:137], v142
	v_cvt_pk_f32_fp8_sdwa v[138:139], v142 src0_sel:WORD_1
	v_cvt_pk_f32_fp8_e32 v[140:141], v143
	v_cvt_pk_f32_fp8_sdwa v[142:143], v143 src0_sel:WORD_1
	v_cvt_pk_f32_fp8_sdwa v[186:187], v190 src0_sel:WORD_1
	v_pk_add_f32 v[154:155], v[154:155], 0 op_sel_hi:[1,0]
	v_pk_add_f32 v[164:165], v[164:165], 0 op_sel_hi:[1,0]
	s_mov_b32 s8, s1
	s_ashr_i32 s1, s0, 31
	v_cvt_pk_f32_fp8_e32 v[144:145], v190
	v_cvt_pk_f32_fp8_e32 v[188:189], v191
	v_cvt_pk_f32_fp8_sdwa v[190:191], v191 src0_sel:WORD_1
	v_pk_add_f32 v[194:195], v[194:195], 0 op_sel_hi:[1,0]
	v_pk_add_f32 v[156:157], v[156:157], 0 op_sel_hi:[1,0]
	v_pk_add_f32 v[158:159], v[158:159], 0 op_sel_hi:[1,0]
	v_pk_add_f32 v[160:161], v[160:161], 0 op_sel_hi:[1,0]
	v_pk_add_f32 v[162:163], v[162:163], 0 op_sel_hi:[1,0]
	v_pk_add_f32 v[166:167], v[166:167], 0 op_sel_hi:[1,0]
	v_pk_add_f32 v[168:169], v[168:169], 0 op_sel_hi:[1,0]
	v_pk_add_f32 v[182:183], v[182:183], 0 op_sel_hi:[1,0]
	v_pk_add_f32 v[66:67], v[154:155], v[66:67]
	v_pk_add_f32 v[76:77], v[164:165], v[76:77]
	s_lshl_b64 s[16:17], s[0:1], 13
	v_pk_add_f32 v[198:199], v[198:199], 0 op_sel_hi:[1,0]
	v_pk_add_f32 v[172:173], v[172:173], 0 op_sel_hi:[1,0]
	v_pk_add_f32 v[180:181], v[180:181], 0 op_sel_hi:[1,0]
	v_pk_add_f32 v[184:185], v[184:185], 0 op_sel_hi:[1,0]
	v_pk_add_f32 v[148:149], v[194:195], v[148:149]
	v_pk_add_f32 v[68:69], v[156:157], v[68:69]
	v_pk_add_f32 v[70:71], v[158:159], v[70:71]
	v_pk_add_f32 v[72:73], v[160:161], v[72:73]
	v_pk_add_f32 v[74:75], v[162:163], v[74:75]
	v_pk_add_f32 v[78:79], v[166:167], v[78:79]
	v_pk_add_f32 v[80:81], v[168:169], v[80:81]
	v_pk_add_f32 v[90:91], v[182:183], v[90:91]
	v_pk_add_f32 v[66:67], v[66:67], v[94:95]
	v_pk_add_f32 v[76:77], v[76:77], v[104:105]
	s_add_u32 s16, s13, s16
	v_pk_add_f32 v[196:197], v[196:197], 0 op_sel_hi:[1,0]
	v_pk_add_f32 v[174:175], v[174:175], 0 op_sel_hi:[1,0]
	v_pk_add_f32 v[152:153], v[198:199], v[152:153]
	v_pk_add_f32 v[84:85], v[172:173], v[84:85]
	v_pk_add_f32 v[88:89], v[180:181], v[88:89]
	v_pk_add_f32 v[92:93], v[184:185], v[92:93]
	v_pk_add_f32 v[148:149], v[148:149], v[170:171]
	v_pk_add_f32 v[68:69], v[68:69], v[96:97]
	v_pk_add_f32 v[70:71], v[70:71], v[98:99]
	v_pk_add_f32 v[72:73], v[72:73], v[100:101]
	v_pk_add_f32 v[74:75], v[74:75], v[102:103]
	v_pk_add_f32 v[78:79], v[78:79], v[106:107]
	v_pk_add_f32 v[80:81], v[80:81], v[108:109]
	v_pk_add_f32 v[90:91], v[90:91], v[116:117]
	v_pk_add_f32 v[66:67], v[66:67], v[120:121]
	v_pk_add_f32 v[76:77], v[76:77], v[130:131]
	s_addc_u32 s17, s14, s17
	v_pk_add_f32 v[150:151], v[196:197], v[150:151]
	v_pk_add_f32 v[86:87], v[174:175], v[86:87]
	v_pk_add_f32 v[152:153], v[152:153], v[178:179]
	v_pk_add_f32 v[84:85], v[84:85], v[110:111]
	v_pk_add_f32 v[88:89], v[88:89], v[114:115]
	v_pk_add_f32 v[92:93], v[92:93], v[118:119]
	v_pk_add_f32 v[94:95], v[148:149], v[186:187]
	v_pk_add_f32 v[68:69], v[68:69], v[122:123]
	v_pk_add_f32 v[70:71], v[70:71], v[124:125]
	v_pk_add_f32 v[72:73], v[72:73], v[126:127]
	v_pk_add_f32 v[74:75], v[74:75], v[128:129]
	v_pk_add_f32 v[78:79], v[78:79], v[132:133]
	v_pk_add_f32 v[80:81], v[80:81], v[134:135]
	v_pk_add_f32 v[90:91], v[90:91], v[142:143]
	v_pk_mul_f32 v[114:115], v[66:67], s[12:13] op_sel_hi:[1,0]
	v_pk_mul_f32 v[130:131], v[76:77], s[12:13] op_sel_hi:[1,0]
	v_lshl_add_u64 v[76:77], s[16:17], 0, v[16:17]
	s_add_u32 s18, s16, 0x1000
	v_pk_add_f32 v[150:151], v[150:151], v[176:177]
	v_pk_add_f32 v[86:87], v[86:87], v[112:113]
	v_pk_add_f32 v[98:99], v[152:153], v[190:191]
	v_pk_add_f32 v[84:85], v[84:85], v[136:137]
	v_pk_add_f32 v[92:93], v[92:93], v[144:145]
	v_pk_mul_f32 v[106:107], v[94:95], s[12:13] op_sel_hi:[1,0]
	v_pk_mul_f32 v[118:119], v[68:69], s[12:13] op_sel_hi:[1,0]
	v_pk_mul_f32 v[122:123], v[70:71], s[12:13] op_sel_hi:[1,0]
	v_pk_mul_f32 v[124:125], v[72:73], s[12:13] op_sel_hi:[1,0]
	v_pk_mul_f32 v[128:129], v[74:75], s[12:13] op_sel_hi:[1,0]
	v_pk_mul_f32 v[132:133], v[78:79], s[12:13] op_sel_hi:[1,0]
	v_pk_mul_f32 v[136:137], v[80:81], s[12:13] op_sel_hi:[1,0]
	v_pk_mul_f32 v[144:145], v[90:91], s[12:13] op_sel_hi:[1,0]
	v_pk_mul_f32 v[78:79], v[114:115], v[114:115]
	global_load_dwordx2 v[74:75], v[76:77], off
	global_load_dwordx2 v[70:71], v[76:77], off offset:512
	global_load_dwordx2 v[68:69], v[76:77], off offset:1024
	global_load_dwordx2 v[66:67], v[76:77], off offset:1536
	global_load_dwordx2 v[72:73], v[76:77], off offset:2048
	global_load_dwordx2 v[80:81], v[76:77], off offset:2560
	global_load_dwordx2 v[90:91], v[76:77], off offset:3072
	global_load_dwordx2 v[94:95], v[76:77], off offset:3584
	s_addc_u32 s19, s17, 0
	v_pk_add_f32 v[96:97], v[150:151], v[188:189]
	v_pk_add_f32 v[86:87], v[86:87], v[138:139]
	v_pk_mul_f32 v[112:113], v[98:99], s[12:13] op_sel_hi:[1,0]
	v_pk_mul_f32 v[138:139], v[84:85], s[12:13] op_sel_hi:[1,0]
	v_pk_mul_f32 v[84:85], v[118:119], v[118:119]
	v_add_f32_e32 v98, v78, v79
	s_add_u32 s16, s16, 0x1800
	v_pk_add_f32 v[88:89], v[88:89], v[140:141]
	v_pk_mul_f32 v[110:111], v[96:97], s[12:13] op_sel_hi:[1,0]
	v_pk_mul_f32 v[140:141], v[86:87], s[12:13] op_sel_hi:[1,0]
	v_lshl_add_u64 v[76:77], s[18:19], 0, v[16:17]
	v_lshl_add_u64 v[78:79], s[18:19], 0, v[20:21]
	v_lshl_add_u64 v[86:87], s[18:19], 0, v[22:23]
	v_lshl_add_u64 v[96:97], s[18:19], 0, v[24:25]
	v_add_f32_e32 v84, v98, v84
	s_addc_u32 s17, s17, 0
	s_lshl_b64 s[0:1], s[0:1], 12
	v_pk_mul_f32 v[154:155], v[122:123], v[122:123]
	global_load_dwordx2 v[100:101], v[76:77], off
	global_load_dwordx2 v[108:109], v[78:79], off
	global_load_dwordx2 v[116:117], v[86:87], off
	global_load_dwordx2 v[120:121], v[96:97], off
	v_add_f32_e32 v96, v85, v84
	v_lshl_add_u64 v[76:77], s[16:17], 0, v[16:17]
	v_lshl_add_u64 v[78:79], s[16:17], 0, v[20:21]
	v_lshl_add_u64 v[84:85], s[16:17], 0, v[22:23]
	v_lshl_add_u64 v[86:87], s[16:17], 0, v[24:25]
	v_lshl_add_u64 v[102:103], v[26:27], 0, s[0:1]
	v_add_f32_e32 v154, v154, v96
	global_load_dwordx2 v[126:127], v[76:77], off
	global_load_dwordx2 v[134:135], v[78:79], off
	global_load_dwordx2 v[142:143], v[84:85], off
	global_load_dwordx2 v[190:191], v[86:87], off
	s_nop 0
	global_load_dwordx4 v[76:79], v[102:103], off nt
	global_load_dwordx4 v[84:87], v[102:103], off offset:1024 nt
	global_load_dwordx4 v[96:99], v[102:103], off offset:2048 nt
	s_nop 0
	global_load_dwordx4 v[102:105], v[102:103], off offset:3072 nt
	v_pk_mul_f32 v[156:157], v[124:125], v[124:125]
	v_add_f32_e32 v154, v155, v154
	v_add_f32_e32 v154, v156, v154
	v_pk_mul_f32 v[158:159], v[128:129], v[128:129]
	v_add_f32_e32 v154, v157, v154
	v_add_f32_e32 v154, v158, v154
	v_pk_mul_f32 v[160:161], v[130:131], v[130:131]
	v_add_f32_e32 v154, v159, v154
	v_add_f32_e32 v154, v160, v154
	v_pk_mul_f32 v[162:163], v[132:133], v[132:133]
	v_add_f32_e32 v154, v161, v154
	v_add_f32_e32 v154, v162, v154
	v_pk_mul_f32 v[164:165], v[136:137], v[136:137]
	v_add_f32_e32 v154, v163, v154
	v_add_f32_e32 v154, v164, v154
	v_pk_mul_f32 v[166:167], v[138:139], v[138:139]
	v_add_f32_e32 v154, v165, v154
	v_add_f32_e32 v154, v166, v154
	v_pk_mul_f32 v[168:169], v[140:141], v[140:141]
	v_add_f32_e32 v154, v167, v154
	v_pk_mul_f32 v[88:89], v[88:89], s[12:13] op_sel_hi:[1,0]
	v_add_f32_e32 v154, v168, v154
	v_pk_mul_f32 v[170:171], v[88:89], v[88:89]
	v_add_f32_e32 v154, v169, v154
	v_add_f32_e32 v154, v170, v154
	v_pk_mul_f32 v[172:173], v[144:145], v[144:145]
	v_add_f32_e32 v154, v171, v154
	v_pk_mul_f32 v[92:93], v[92:93], s[12:13] op_sel_hi:[1,0]
	v_add_f32_e32 v154, v172, v154
	v_pk_mul_f32 v[174:175], v[92:93], v[92:93]
	v_add_f32_e32 v154, v173, v154
	v_add_f32_e32 v154, v174, v154
	v_pk_mul_f32 v[148:149], v[106:107], v[106:107]
	v_add_f32_e32 v154, v175, v154
	v_add_f32_e32 v148, v148, v154
	v_pk_mul_f32 v[150:151], v[110:111], v[110:111]
	v_add_f32_e32 v148, v149, v148
	v_add_f32_e32 v148, v150, v148
	v_pk_mul_f32 v[152:153], v[112:113], v[112:113]
	v_add_f32_e32 v148, v151, v148
	v_add_f32_e32 v148, v152, v148
	v_add_f32_e32 v148, v153, v148
	v_lshlrev_b32_e32 v62, 16, v12
	v_and_b32_e32 v63, 0xffff0000, v12
	v_add_f32_dpp v148, v148, v148 quad_perm:[1,0,3,2] row_mask:0xf bank_mask:0xf bound_ctrl:1
	v_lshlrev_b32_e32 v12, 16, v13
	v_and_b32_e32 v13, 0xffff0000, v13
	v_add_f32_dpp v148, v148, v148 quad_perm:[2,3,0,1] row_mask:0xf bank_mask:0xf bound_ctrl:1
	v_lshlrev_b32_e32 v64, 16, v14
	v_and_b32_e32 v65, 0xffff0000, v14
	v_add_f32_dpp v148, v148, v148 row_ror:4 row_mask:0xf bank_mask:0xf bound_ctrl:1
	v_lshlrev_b32_e32 v14, 16, v15
	v_and_b32_e32 v15, 0xffff0000, v15
	v_add_f32_dpp v148, v148, v148 row_ror:8 row_mask:0xf bank_mask:0xf bound_ctrl:1
	v_lshlrev_b32_e32 v82, 16, v8
	v_readlane_b32 s9, v148, 16
	v_readlane_b32 s15, v148, 48
	v_readlane_b32 s0, v148, 0
	v_readlane_b32 s1, v148, 32
	v_mov_b32_e32 v148, s9
	v_mov_b32_e32 v149, s15
	v_pk_add_f32 v[148:149], s[0:1], v[148:149]
	v_and_b32_e32 v83, 0xffff0000, v8
	v_add_f32_e32 v148, v148, v149
	v_fmamk_f32 v148, v148, 0x3a000000, v19
	v_mul_f32_e32 v149, 0x4b800000, v148
	v_cmp_gt_f32_e64 s[0:1], s3, v148
	v_lshlrev_b32_e32 v8, 16, v9
	v_and_b32_e32 v9, 0xffff0000, v9
	v_cndmask_b32_e64 v148, v148, v149, s[0:1]
	v_rsq_f32_e32 v148, v148
	v_lshlrev_b32_e32 v146, 16, v10
	v_and_b32_e32 v147, 0xffff0000, v10
	v_lshlrev_b32_e32 v10, 16, v11
	v_mul_f32_e32 v149, 0x45800000, v148
	v_cndmask_b32_e64 v148, v148, v149, s[0:1]
	v_and_b32_e32 v11, 0xffff0000, v11
	v_lshlrev_b32_e32 v192, 16, v4
	v_and_b32_e32 v193, 0xffff0000, v4
	v_lshlrev_b32_e32 v4, 16, v5
	v_and_b32_e32 v5, 0xffff0000, v5
	v_lshlrev_b32_e32 v200, 16, v6
	v_and_b32_e32 v201, 0xffff0000, v6
	v_lshlrev_b32_e32 v6, 16, v7
	v_and_b32_e32 v7, 0xffff0000, v7
	v_lshlrev_b32_e32 v202, 16, v0
	v_and_b32_e32 v203, 0xffff0000, v0
	v_lshlrev_b32_e32 v0, 16, v1
	v_and_b32_e32 v1, 0xffff0000, v1
	v_lshlrev_b32_e32 v204, 16, v2
	v_and_b32_e32 v205, 0xffff0000, v2
	v_lshlrev_b32_e32 v2, 16, v3
	v_and_b32_e32 v3, 0xffff0000, v3
	v_pk_mul_f32 v[114:115], v[114:115], v[148:149] op_sel_hi:[1,0]
	v_pk_mul_f32 v[118:119], v[118:119], v[148:149] op_sel_hi:[1,0]
	v_pk_mul_f32 v[122:123], v[122:123], v[148:149] op_sel_hi:[1,0]
	v_pk_mul_f32 v[124:125], v[124:125], v[148:149] op_sel_hi:[1,0]
	v_pk_mul_f32 v[128:129], v[128:129], v[148:149] op_sel_hi:[1,0]
	v_pk_mul_f32 v[130:131], v[130:131], v[148:149] op_sel_hi:[1,0]
	v_pk_mul_f32 v[132:133], v[132:133], v[148:149] op_sel_hi:[1,0]
	v_pk_mul_f32 v[136:137], v[136:137], v[148:149] op_sel_hi:[1,0]
	v_pk_mul_f32 v[138:139], v[138:139], v[148:149] op_sel_hi:[1,0]
	v_pk_mul_f32 v[140:141], v[140:141], v[148:149] op_sel_hi:[1,0]
	v_pk_mul_f32 v[88:89], v[88:89], v[148:149] op_sel_hi:[1,0]
	v_pk_mul_f32 v[144:145], v[144:145], v[148:149] op_sel_hi:[1,0]
	v_pk_mul_f32 v[92:93], v[92:93], v[148:149] op_sel_hi:[1,0]
	v_pk_mul_f32 v[106:107], v[106:107], v[148:149] op_sel_hi:[1,0]
	v_pk_mul_f32 v[150:151], v[110:111], v[148:149] op_sel_hi:[1,0]
	v_pk_mul_f32 v[148:149], v[112:113], v[148:149] op_sel_hi:[1,0]
	v_pk_fma_f32 v[110:111], v[30:31], v[114:115], v[62:63]
	v_pk_fma_f32 v[112:113], v[28:29], v[118:119], v[12:13]
	v_pk_fma_f32 v[12:13], v[34:35], v[122:123], v[64:65]
	v_pk_fma_f32 v[14:15], v[32:33], v[124:125], v[14:15]
	v_pk_fma_f32 v[64:65], v[36:37], v[130:131], v[8:9]
	v_pk_fma_f32 v[8:9], v[42:43], v[132:133], v[146:147]
	v_pk_fma_f32 v[10:11], v[40:41], v[136:137], v[10:11]
	v_pk_fma_f32 v[124:125], v[44:45], v[140:141], v[4:5]
	v_pk_fma_f32 v[4:5], v[50:51], v[88:89], v[200:201]
	v_pk_fma_f32 v[6:7], v[48:49], v[144:145], v[6:7]
	v_pk_fma_f32 v[130:131], v[52:53], v[106:107], v[0:1]
	v_pk_fma_f32 v[0:1], v[58:59], v[150:151], v[204:205]
	v_pk_fma_f32 v[2:3], v[56:57], v[148:149], v[2:3]
	v_pk_fma_f32 v[62:63], v[38:39], v[128:129], v[82:83]
	v_pk_fma_f32 v[122:123], v[46:47], v[138:139], v[192:193]
	v_pk_fma_f32 v[128:129], v[54:55], v[92:93], v[202:203]
	global_store_dwordx4 v[60:61], v[110:113], off offset:-4096
	global_store_dwordx4 v[60:61], v[12:15], off offset:-4080
	global_store_dwordx4 v[60:61], v[62:65], off offset:-2048
	global_store_dwordx4 v[60:61], v[8:11], off offset:-2032
	global_store_dwordx4 v[60:61], v[122:125], off
	global_store_dwordx4 v[60:61], v[4:7], off offset:16
	global_store_dwordx4 v[60:61], v[128:131], off offset:2048
	global_store_dwordx4 v[60:61], v[0:3], off offset:2064
	s_waitcnt vmcnt(9)
	v_mov_b64_e32 v[4:5], v[96:97]
	v_mov_b64_e32 v[8:9], v[84:85]
	s_waitcnt vmcnt(8)
	v_mov_b64_e32 v[0:1], v[102:103]
	v_mov_b64_e32 v[12:13], v[76:77]
	v_lshl_add_u64 v[60:61], v[60:61], 0, s[10:11]
	v_mov_b64_e32 v[2:3], v[104:105]
	v_mov_b64_e32 v[6:7], v[98:99]
	v_mov_b64_e32 v[10:11], v[86:87]
	v_mov_b64_e32 v[14:15], v[78:79]
	s_cbranch_vccnz .LBB0_1339

.LBB0_1342:
	s_cmpk_gt_i32 s4, 0x3fff
	s_cbranch_scc1 .LBB0_1345
	s_add_u32 s0, s92, 0x296000
	v_readlane_b32 s16, v253, 29
	s_waitcnt vmcnt(6)
	v_or_b32_e32 v20, 0x200, v16
	s_addc_u32 s1, s93, 0
	v_readlane_b32 s17, v253, 30
	v_lshlrev_b32_e32 v0, 2, v20
	v_or_b32_e32 v22, 0x400, v16
	global_load_dwordx4 v[32:35], v207, s[0:1] offset:16 nt
	global_load_dwordx4 v[28:31], v207, s[0:1] nt
	s_nop 0
	global_load_dwordx4 v[36:39], v207, s[16:17] offset:16 nt
	global_load_dwordx4 v[40:43], v207, s[16:17] nt
	global_load_dwordx4 v[44:47], v0, s[0:1] offset:16 nt
	global_load_dwordx4 v[48:51], v0, s[0:1] nt
	global_load_dwordx4 v[52:55], v207, s[16:17] offset:2064 nt
	global_load_dwordx4 v[56:59], v207, s[16:17] offset:2048 nt
	v_lshlrev_b32_e32 v0, 2, v22
	v_or_b32_e32 v24, 0x600, v16
	global_load_dwordx4 v[60:63], v0, s[0:1] offset:16 nt
	global_load_dwordx4 v[74:77], v0, s[0:1] nt
	global_load_dwordx4 v[80:83], v0, s[16:17] offset:16 nt
	global_load_dwordx4 v[84:87], v0, s[16:17] nt
	v_lshlrev_b32_e32 v0, 2, v24
	s_ashr_i32 s5, s4, 31
	global_load_dwordx4 v[94:97], v0, s[0:1] offset:16 nt
	global_load_dwordx4 v[100:103], v0, s[0:1] nt
	global_load_dwordx4 v[108:111], v0, s[16:17] offset:16 nt
	global_load_dwordx4 v[120:123], v0, s[16:17] nt
	s_lshl_b64 s[0:1], s[4:5], 12
	s_add_u32 s0, s6, s0
	s_addc_u32 s1, s7, s1
	s_mov_b64 s[8:9], s[16:17]
	global_load_dwordx4 v[0:3], v18, s[0:1] offset:3072 nt
	global_load_dwordx4 v[4:7], v18, s[0:1] offset:2048 nt
	global_load_dwordx4 v[8:11], v18, s[0:1] offset:1024 nt
	global_load_dwordx4 v[12:15], v18, s[0:1] nt
	s_lshl_b64 s[0:1], s[4:5], 13
	s_add_u32 s8, s13, s0
	s_addc_u32 s9, s14, s1
	s_add_u32 s10, s8, 0x1800
	s_addc_u32 s11, s9, 0
	s_add_u32 s16, s8, 0x1000
	s_addc_u32 s17, s9, 0
	global_load_dwordx2 v[188:189], v24, s[10:11]
	global_load_dwordx2 v[140:141], v22, s[10:11]
	global_load_dwordx2 v[114:115], v22, s[16:17]
	global_load_dwordx2 v[118:119], v24, s[16:17]
	global_load_dwordx2 v[124:125], v16, s[10:11]
	global_load_dwordx2 v[98:99], v16, s[16:17]
	global_load_dwordx2 v[92:93], v16, s[8:9] offset:3584
	global_load_dwordx2 v[88:89], v16, s[8:9] offset:3072
	global_load_dwordx2 v[78:79], v16, s[8:9] offset:2560
	global_load_dwordx2 v[70:71], v16, s[8:9] offset:2048
	global_load_dwordx2 v[64:65], v16, s[8:9] offset:1536
	global_load_dwordx2 v[66:67], v16, s[8:9] offset:1024
	global_load_dwordx2 v[132:133], v20, s[10:11]
	global_load_dwordx2 v[106:107], v20, s[16:17]
	global_load_dwordx2 v[68:69], v16, s[8:9] offset:512
	global_load_dwordx2 v[72:73], v16, s[8:9]
	v_mov_b32_e32 v17, 0
	s_add_u32 s0, s50, s0
	v_lshlrev_b32_e32 v90, 5, v206
	v_mov_b32_e32 v91, v17
	s_addc_u32 s1, s51, s1
	s_mov_b64 s[8:9], 0x1000
	v_mov_b32_e32 v19, v17
	s_ashr_i32 s3, s2, 31
	v_mov_b32_e32 v21, v17
	v_mov_b32_e32 v23, v17
	v_mov_b32_e32 v25, v17
	v_lshl_add_u64 v[18:19], s[6:7], 0, v[18:19]
	s_lshl_b64 s[6:7], s[2:3], 13
	v_mov_b32_e32 v204, 0x358637bd
	s_mov_b32 s3, 0x800000
	v_readlane_b32 s18, v253, 31
	v_readlane_b32 s19, v253, 32
	v_readlane_b32 s20, v253, 33
	v_readlane_b32 s21, v253, 34
	v_readlane_b32 s22, v253, 35
	v_readlane_b32 s23, v253, 36
	v_readlane_b32 s24, v253, 37
	v_readlane_b32 s25, v253, 38
	v_readlane_b32 s26, v253, 39
	v_readlane_b32 s27, v253, 40
	v_readlane_b32 s28, v253, 41
	v_readlane_b32 s29, v253, 42
	v_readlane_b32 s30, v253, 43
	v_readlane_b32 s31, v253, 44
	s_waitcnt vmcnt(33)
	v_pk_mul_f32 v[32:33], v[32:33], v[36:37]
	s_waitcnt vmcnt(32)
	v_pk_mul_f32 v[26:27], v[30:31], v[42:43]
	v_pk_mul_f32 v[30:31], v[34:35], v[38:39]
	s_waitcnt vmcnt(28)
	v_pk_mul_f32 v[34:35], v[50:51], v[58:59]
	v_lshl_add_u64 v[58:59], s[0:1], 0, v[90:91]
	v_pk_mul_f32 v[28:29], v[28:29], v[40:41]
	v_pk_mul_f32 v[36:37], v[48:49], v[56:57]
	v_pk_mul_f32 v[38:39], v[46:47], v[54:55]
	v_pk_mul_f32 v[40:41], v[44:45], v[52:53]
	s_waitcnt vmcnt(24)
	v_pk_mul_f32 v[42:43], v[76:77], v[86:87]
	v_pk_mul_f32 v[44:45], v[74:75], v[84:85]
	v_pk_mul_f32 v[46:47], v[62:63], v[82:83]
	v_pk_mul_f32 v[48:49], v[60:61], v[80:81]
	s_waitcnt vmcnt(20)
	v_pk_mul_f32 v[50:51], v[102:103], v[122:123]
	v_pk_mul_f32 v[52:53], v[100:101], v[120:121]
	v_pk_mul_f32 v[54:55], v[96:97], v[110:111]
	v_pk_mul_f32 v[56:57], v[94:95], v[108:109]
	v_lshl_add_u64 v[58:59], v[58:59], 0, s[8:9]
	s_mov_b32 s8, 0x3d800000
.LBB0_1344:
	s_add_i32 s1, s4, s2
	s_waitcnt vmcnt(0)
	v_cvt_pk_f32_fp8_e32 v[152:153], v72
	v_cvt_pk_f32_fp8_sdwa v[162:163], v68 src0_sel:WORD_1
	s_cmpk_lt_i32 s1, 0x4000
	v_cvt_pk_f32_fp8_sdwa v[154:155], v72 src0_sel:WORD_1
	v_cvt_pk_f32_fp8_e32 v[156:157], v73
	v_cvt_pk_f32_fp8_sdwa v[158:159], v73 src0_sel:WORD_1
	v_cvt_pk_f32_fp8_e32 v[160:161], v68
	v_cvt_pk_f32_fp8_e32 v[164:165], v69
	v_cvt_pk_f32_fp8_sdwa v[166:167], v69 src0_sel:WORD_1
	v_cvt_pk_f32_fp8_sdwa v[180:181], v67 src0_sel:WORD_1
	v_cvt_pk_f32_fp8_e32 v[182:183], v64
	v_cvt_pk_f32_fp8_sdwa v[192:193], v64 src0_sel:WORD_1
	v_cvt_pk_f32_fp8_e32 v[194:195], v65
	v_cvt_pk_f32_fp8_sdwa v[196:197], v65 src0_sel:WORD_1
	v_cvt_pk_f32_fp8_e32 v[64:65], v70
	v_cvt_pk_f32_fp8_sdwa v[74:75], v78 src0_sel:WORD_1
	s_cselect_b64 s[10:11], -1, 0
	v_cvt_pk_f32_fp8_e32 v[170:171], v66
	v_cvt_pk_f32_fp8_sdwa v[172:173], v66 src0_sel:WORD_1
	v_cvt_pk_f32_fp8_e32 v[178:179], v67
	v_cvt_pk_f32_fp8_sdwa v[66:67], v70 src0_sel:WORD_1
	v_cvt_pk_f32_fp8_e32 v[68:69], v71
	v_cvt_pk_f32_fp8_sdwa v[70:71], v71 src0_sel:WORD_1
	v_cvt_pk_f32_fp8_e32 v[72:73], v78
	v_cvt_pk_f32_fp8_e32 v[76:77], v79
	v_cvt_pk_f32_fp8_sdwa v[78:79], v79 src0_sel:WORD_1
	v_cvt_pk_f32_fp8_e32 v[82:83], v88
	v_cvt_pk_f32_fp8_sdwa v[84:85], v88 src0_sel:WORD_1
	v_cvt_pk_f32_fp8_e32 v[86:87], v89
	v_cvt_pk_f32_fp8_sdwa v[88:89], v89 src0_sel:WORD_1
	v_cvt_pk_f32_fp8_e32 v[90:91], v92
	v_cvt_pk_f32_fp8_sdwa v[146:147], v92 src0_sel:WORD_1
	v_cvt_pk_f32_fp8_e32 v[148:149], v93
	v_cvt_pk_f32_fp8_sdwa v[150:151], v93 src0_sel:WORD_1
	v_cvt_pk_f32_fp8_e32 v[92:93], v98
	v_cvt_pk_f32_fp8_sdwa v[102:103], v106 src0_sel:WORD_1
	s_and_b64 vcc, s[10:11], exec
	v_cvt_pk_f32_fp8_sdwa v[94:95], v98 src0_sel:WORD_1
	v_cvt_pk_f32_fp8_e32 v[96:97], v99
	v_cvt_pk_f32_fp8_sdwa v[98:99], v99 src0_sel:WORD_1
	v_cvt_pk_f32_fp8_e32 v[100:101], v106
	v_cvt_pk_f32_fp8_e32 v[104:105], v107
	v_cvt_pk_f32_fp8_sdwa v[106:107], v107 src0_sel:WORD_1
	v_cvt_pk_f32_fp8_e32 v[108:109], v114
	v_cvt_pk_f32_fp8_sdwa v[110:111], v114 src0_sel:WORD_1
	v_cvt_pk_f32_fp8_e32 v[112:113], v115
	v_cvt_pk_f32_fp8_sdwa v[114:115], v115 src0_sel:WORD_1
	v_cvt_pk_f32_fp8_e32 v[116:117], v118
	v_cvt_pk_f32_fp8_sdwa v[168:169], v118 src0_sel:WORD_1
	v_cvt_pk_f32_fp8_e32 v[174:175], v119
	v_cvt_pk_f32_fp8_sdwa v[176:177], v119 src0_sel:WORD_1
	v_cvt_pk_f32_fp8_e32 v[118:119], v124
	v_cvt_pk_f32_fp8_sdwa v[128:129], v132 src0_sel:WORD_1
	s_cselect_b32 s0, s1, s4
	v_cvt_pk_f32_fp8_sdwa v[120:121], v124 src0_sel:WORD_1
	v_cvt_pk_f32_fp8_e32 v[122:123], v125
	v_cvt_pk_f32_fp8_sdwa v[124:125], v125 src0_sel:WORD_1
	v_cvt_pk_f32_fp8_e32 v[126:127], v132
	v_cvt_pk_f32_fp8_e32 v[130:131], v133
	v_cvt_pk_f32_fp8_sdwa v[132:133], v133 src0_sel:WORD_1
	v_cvt_pk_f32_fp8_e32 v[134:135], v140
	v_cvt_pk_f32_fp8_sdwa v[136:137], v140 src0_sel:WORD_1
	v_cvt_pk_f32_fp8_e32 v[138:139], v141
	v_cvt_pk_f32_fp8_sdwa v[140:141], v141 src0_sel:WORD_1
	v_cvt_pk_f32_fp8_sdwa v[184:185], v188 src0_sel:WORD_1
	v_pk_add_f32 v[152:153], v[152:153], 0 op_sel_hi:[1,0]
	v_pk_add_f32 v[162:163], v[162:163], 0 op_sel_hi:[1,0]
	s_mov_b32 s4, s1
	s_ashr_i32 s1, s0, 31
	v_cvt_pk_f32_fp8_e32 v[142:143], v188
	v_cvt_pk_f32_fp8_e32 v[186:187], v189
	v_cvt_pk_f32_fp8_sdwa v[188:189], v189 src0_sel:WORD_1
	v_pk_add_f32 v[192:193], v[192:193], 0 op_sel_hi:[1,0]
	v_pk_add_f32 v[154:155], v[154:155], 0 op_sel_hi:[1,0]
	v_pk_add_f32 v[156:157], v[156:157], 0 op_sel_hi:[1,0]
	v_pk_add_f32 v[158:159], v[158:159], 0 op_sel_hi:[1,0]
	v_pk_add_f32 v[160:161], v[160:161], 0 op_sel_hi:[1,0]
	v_pk_add_f32 v[164:165], v[164:165], 0 op_sel_hi:[1,0]
	v_pk_add_f32 v[166:167], v[166:167], 0 op_sel_hi:[1,0]
	v_pk_add_f32 v[180:181], v[180:181], 0 op_sel_hi:[1,0]
	v_pk_add_f32 v[64:65], v[152:153], v[64:65]
	v_pk_add_f32 v[74:75], v[162:163], v[74:75]
	s_lshl_b64 s[10:11], s[0:1], 13
	v_pk_add_f32 v[196:197], v[196:197], 0 op_sel_hi:[1,0]
	v_pk_add_f32 v[170:171], v[170:171], 0 op_sel_hi:[1,0]
	v_pk_add_f32 v[178:179], v[178:179], 0 op_sel_hi:[1,0]
	v_pk_add_f32 v[182:183], v[182:183], 0 op_sel_hi:[1,0]
	v_pk_add_f32 v[146:147], v[192:193], v[146:147]
	v_pk_add_f32 v[66:67], v[154:155], v[66:67]
	v_pk_add_f32 v[68:69], v[156:157], v[68:69]
	v_pk_add_f32 v[70:71], v[158:159], v[70:71]
	v_pk_add_f32 v[72:73], v[160:161], v[72:73]
	v_pk_add_f32 v[76:77], v[164:165], v[76:77]
	v_pk_add_f32 v[78:79], v[166:167], v[78:79]
	v_pk_add_f32 v[88:89], v[180:181], v[88:89]
	v_pk_add_f32 v[64:65], v[64:65], v[92:93]
	v_pk_add_f32 v[74:75], v[74:75], v[102:103]
	s_add_u32 s10, s13, s10
	v_pk_add_f32 v[194:195], v[194:195], 0 op_sel_hi:[1,0]
	v_pk_add_f32 v[172:173], v[172:173], 0 op_sel_hi:[1,0]
	v_pk_add_f32 v[150:151], v[196:197], v[150:151]
	v_pk_add_f32 v[82:83], v[170:171], v[82:83]
	v_pk_add_f32 v[86:87], v[178:179], v[86:87]
	v_pk_add_f32 v[90:91], v[182:183], v[90:91]
	v_pk_add_f32 v[146:147], v[146:147], v[168:169]
	v_pk_add_f32 v[66:67], v[66:67], v[94:95]
	v_pk_add_f32 v[68:69], v[68:69], v[96:97]
	v_pk_add_f32 v[70:71], v[70:71], v[98:99]
	v_pk_add_f32 v[72:73], v[72:73], v[100:101]
	v_pk_add_f32 v[76:77], v[76:77], v[104:105]
	v_pk_add_f32 v[78:79], v[78:79], v[106:107]
	v_pk_add_f32 v[88:89], v[88:89], v[114:115]
	v_pk_add_f32 v[64:65], v[64:65], v[118:119]
	v_pk_add_f32 v[74:75], v[74:75], v[128:129]
	s_addc_u32 s11, s14, s11
	v_pk_add_f32 v[148:149], v[194:195], v[148:149]
	v_pk_add_f32 v[84:85], v[172:173], v[84:85]
	v_pk_add_f32 v[150:151], v[150:151], v[176:177]
	v_pk_add_f32 v[82:83], v[82:83], v[108:109]
	v_pk_add_f32 v[86:87], v[86:87], v[112:113]
	v_pk_add_f32 v[90:91], v[90:91], v[116:117]
	v_pk_add_f32 v[92:93], v[146:147], v[184:185]
	v_pk_add_f32 v[66:67], v[66:67], v[120:121]
	v_pk_add_f32 v[68:69], v[68:69], v[122:123]
	v_pk_add_f32 v[70:71], v[70:71], v[124:125]
	v_pk_add_f32 v[72:73], v[72:73], v[126:127]
	v_pk_add_f32 v[76:77], v[76:77], v[130:131]
	v_pk_add_f32 v[78:79], v[78:79], v[132:133]
	v_pk_add_f32 v[88:89], v[88:89], v[140:141]
	v_pk_mul_f32 v[112:113], v[64:65], s[8:9] op_sel_hi:[1,0]
	v_pk_mul_f32 v[128:129], v[74:75], s[8:9] op_sel_hi:[1,0]
	v_lshl_add_u64 v[74:75], s[10:11], 0, v[16:17]
	s_add_u32 s16, s10, 0x1000
	v_pk_add_f32 v[148:149], v[148:149], v[174:175]
	v_pk_add_f32 v[84:85], v[84:85], v[110:111]
	v_pk_add_f32 v[96:97], v[150:151], v[188:189]
	v_pk_add_f32 v[82:83], v[82:83], v[134:135]
	v_pk_add_f32 v[90:91], v[90:91], v[142:143]
	v_pk_mul_f32 v[104:105], v[92:93], s[8:9] op_sel_hi:[1,0]
	v_pk_mul_f32 v[116:117], v[66:67], s[8:9] op_sel_hi:[1,0]
	v_pk_mul_f32 v[120:121], v[68:69], s[8:9] op_sel_hi:[1,0]
	v_pk_mul_f32 v[122:123], v[70:71], s[8:9] op_sel_hi:[1,0]
	v_pk_mul_f32 v[126:127], v[72:73], s[8:9] op_sel_hi:[1,0]
	v_pk_mul_f32 v[130:131], v[76:77], s[8:9] op_sel_hi:[1,0]
	v_pk_mul_f32 v[134:135], v[78:79], s[8:9] op_sel_hi:[1,0]
	v_pk_mul_f32 v[142:143], v[88:89], s[8:9] op_sel_hi:[1,0]
	v_pk_mul_f32 v[76:77], v[112:113], v[112:113]
	global_load_dwordx2 v[72:73], v[74:75], off
	global_load_dwordx2 v[68:69], v[74:75], off offset:512
	global_load_dwordx2 v[66:67], v[74:75], off offset:1024
	global_load_dwordx2 v[64:65], v[74:75], off offset:1536
	global_load_dwordx2 v[70:71], v[74:75], off offset:2048
	global_load_dwordx2 v[78:79], v[74:75], off offset:2560
	global_load_dwordx2 v[88:89], v[74:75], off offset:3072
	global_load_dwordx2 v[92:93], v[74:75], off offset:3584
	s_addc_u32 s17, s11, 0
	v_pk_add_f32 v[94:95], v[148:149], v[186:187]
	v_pk_add_f32 v[84:85], v[84:85], v[136:137]
	v_pk_mul_f32 v[110:111], v[96:97], s[8:9] op_sel_hi:[1,0]
	v_pk_mul_f32 v[136:137], v[82:83], s[8:9] op_sel_hi:[1,0]
	v_pk_mul_f32 v[82:83], v[116:117], v[116:117]
	v_add_f32_e32 v96, v76, v77
	s_add_u32 s10, s10, 0x1800
	v_pk_add_f32 v[86:87], v[86:87], v[138:139]
	v_pk_mul_f32 v[108:109], v[94:95], s[8:9] op_sel_hi:[1,0]
	v_pk_mul_f32 v[138:139], v[84:85], s[8:9] op_sel_hi:[1,0]
	v_lshl_add_u64 v[74:75], s[16:17], 0, v[16:17]
	v_lshl_add_u64 v[76:77], s[16:17], 0, v[20:21]
	v_lshl_add_u64 v[84:85], s[16:17], 0, v[22:23]
	v_lshl_add_u64 v[94:95], s[16:17], 0, v[24:25]
	v_add_f32_e32 v82, v96, v82
	s_addc_u32 s11, s11, 0
	s_lshl_b64 s[0:1], s[0:1], 12
	v_pk_mul_f32 v[152:153], v[120:121], v[120:121]
	global_load_dwordx2 v[98:99], v[74:75], off
	global_load_dwordx2 v[106:107], v[76:77], off
	global_load_dwordx2 v[114:115], v[84:85], off
	global_load_dwordx2 v[118:119], v[94:95], off
	v_add_f32_e32 v94, v83, v82
	v_lshl_add_u64 v[74:75], s[10:11], 0, v[16:17]
	v_lshl_add_u64 v[76:77], s[10:11], 0, v[20:21]
	v_lshl_add_u64 v[82:83], s[10:11], 0, v[22:23]
	v_lshl_add_u64 v[84:85], s[10:11], 0, v[24:25]
	v_lshl_add_u64 v[100:101], v[18:19], 0, s[0:1]
	v_add_f32_e32 v152, v152, v94
	global_load_dwordx2 v[124:125], v[74:75], off
	global_load_dwordx2 v[132:133], v[76:77], off
	global_load_dwordx2 v[140:141], v[82:83], off
	global_load_dwordx2 v[188:189], v[84:85], off
	s_nop 0
	global_load_dwordx4 v[74:77], v[100:101], off nt
	global_load_dwordx4 v[82:85], v[100:101], off offset:1024 nt
	global_load_dwordx4 v[94:97], v[100:101], off offset:2048 nt
	s_nop 0
	global_load_dwordx4 v[100:103], v[100:101], off offset:3072 nt
	v_pk_mul_f32 v[154:155], v[122:123], v[122:123]
	v_add_f32_e32 v152, v153, v152
	v_add_f32_e32 v152, v154, v152
	v_pk_mul_f32 v[156:157], v[126:127], v[126:127]
	v_add_f32_e32 v152, v155, v152
	v_add_f32_e32 v152, v156, v152
	v_pk_mul_f32 v[158:159], v[128:129], v[128:129]
	v_add_f32_e32 v152, v157, v152
	v_add_f32_e32 v152, v158, v152
	v_pk_mul_f32 v[160:161], v[130:131], v[130:131]
	v_add_f32_e32 v152, v159, v152
	v_add_f32_e32 v152, v160, v152
	v_pk_mul_f32 v[162:163], v[134:135], v[134:135]
	v_add_f32_e32 v152, v161, v152
	v_add_f32_e32 v152, v162, v152
	v_pk_mul_f32 v[164:165], v[136:137], v[136:137]
	v_add_f32_e32 v152, v163, v152
	v_add_f32_e32 v152, v164, v152
	v_pk_mul_f32 v[166:167], v[138:139], v[138:139]
	v_add_f32_e32 v152, v165, v152
	v_pk_mul_f32 v[86:87], v[86:87], s[8:9] op_sel_hi:[1,0]
	v_add_f32_e32 v152, v166, v152
	v_pk_mul_f32 v[168:169], v[86:87], v[86:87]
	v_add_f32_e32 v152, v167, v152
	v_add_f32_e32 v152, v168, v152
	v_pk_mul_f32 v[170:171], v[142:143], v[142:143]
	v_add_f32_e32 v152, v169, v152
	v_pk_mul_f32 v[90:91], v[90:91], s[8:9] op_sel_hi:[1,0]
	v_add_f32_e32 v152, v170, v152
	v_pk_mul_f32 v[172:173], v[90:91], v[90:91]
	v_add_f32_e32 v152, v171, v152
	v_add_f32_e32 v152, v172, v152
	v_pk_mul_f32 v[146:147], v[104:105], v[104:105]
	v_add_f32_e32 v152, v173, v152
	v_add_f32_e32 v146, v146, v152
	v_pk_mul_f32 v[148:149], v[108:109], v[108:109]
	v_add_f32_e32 v146, v147, v146
	v_add_f32_e32 v146, v148, v146
	v_pk_mul_f32 v[150:151], v[110:111], v[110:111]
	v_add_f32_e32 v146, v149, v146
	v_add_f32_e32 v146, v150, v146
	v_add_f32_e32 v146, v151, v146
	v_lshlrev_b32_e32 v60, 16, v12
	v_and_b32_e32 v61, 0xffff0000, v12
	v_add_f32_dpp v146, v146, v146 quad_perm:[1,0,3,2] row_mask:0xf bank_mask:0xf bound_ctrl:1
	v_lshlrev_b32_e32 v12, 16, v13
	v_and_b32_e32 v13, 0xffff0000, v13
	v_add_f32_dpp v146, v146, v146 quad_perm:[2,3,0,1] row_mask:0xf bank_mask:0xf bound_ctrl:1
	v_lshlrev_b32_e32 v62, 16, v14
	v_and_b32_e32 v63, 0xffff0000, v14
	v_add_f32_dpp v146, v146, v146 row_ror:4 row_mask:0xf bank_mask:0xf bound_ctrl:1
	v_lshlrev_b32_e32 v14, 16, v15
	v_and_b32_e32 v15, 0xffff0000, v15
	v_add_f32_dpp v146, v146, v146 row_ror:8 row_mask:0xf bank_mask:0xf bound_ctrl:1
	v_lshlrev_b32_e32 v80, 16, v8
	v_readlane_b32 s5, v146, 16
	v_readlane_b32 s9, v146, 48
	v_readlane_b32 s0, v146, 0
	v_readlane_b32 s1, v146, 32
	v_mov_b32_e32 v146, s5
	v_mov_b32_e32 v147, s9
	v_pk_add_f32 v[146:147], s[0:1], v[146:147]
	v_and_b32_e32 v81, 0xffff0000, v8
	v_add_f32_e32 v146, v146, v147
	v_fmamk_f32 v146, v146, 0x3a000000, v204
	v_mul_f32_e32 v147, 0x4b800000, v146
	v_cmp_gt_f32_e64 s[0:1], s3, v146
	v_lshlrev_b32_e32 v8, 16, v9
	v_and_b32_e32 v9, 0xffff0000, v9
	v_cndmask_b32_e64 v146, v146, v147, s[0:1]
	v_rsq_f32_e32 v146, v146
	v_lshlrev_b32_e32 v144, 16, v10
	v_and_b32_e32 v145, 0xffff0000, v10
	v_lshlrev_b32_e32 v10, 16, v11
	v_mul_f32_e32 v147, 0x45800000, v146
	v_cndmask_b32_e64 v146, v146, v147, s[0:1]
	v_and_b32_e32 v11, 0xffff0000, v11
	v_lshlrev_b32_e32 v190, 16, v4
	v_and_b32_e32 v191, 0xffff0000, v4
	v_lshlrev_b32_e32 v4, 16, v5
	v_and_b32_e32 v5, 0xffff0000, v5
	v_lshlrev_b32_e32 v198, 16, v6
	v_and_b32_e32 v199, 0xffff0000, v6
	v_lshlrev_b32_e32 v6, 16, v7
	v_and_b32_e32 v7, 0xffff0000, v7
	v_lshlrev_b32_e32 v200, 16, v0
	v_and_b32_e32 v201, 0xffff0000, v0
	v_lshlrev_b32_e32 v0, 16, v1
	v_and_b32_e32 v1, 0xffff0000, v1
	v_lshlrev_b32_e32 v202, 16, v2
	v_and_b32_e32 v203, 0xffff0000, v2
	v_lshlrev_b32_e32 v2, 16, v3
	v_and_b32_e32 v3, 0xffff0000, v3
	v_pk_mul_f32 v[112:113], v[112:113], v[146:147] op_sel_hi:[1,0]
	v_pk_mul_f32 v[116:117], v[116:117], v[146:147] op_sel_hi:[1,0]
	v_pk_mul_f32 v[120:121], v[120:121], v[146:147] op_sel_hi:[1,0]
	v_pk_mul_f32 v[122:123], v[122:123], v[146:147] op_sel_hi:[1,0]
	v_pk_mul_f32 v[126:127], v[126:127], v[146:147] op_sel_hi:[1,0]
	v_pk_mul_f32 v[128:129], v[128:129], v[146:147] op_sel_hi:[1,0]
	v_pk_mul_f32 v[130:131], v[130:131], v[146:147] op_sel_hi:[1,0]
	v_pk_mul_f32 v[134:135], v[134:135], v[146:147] op_sel_hi:[1,0]
	v_pk_mul_f32 v[136:137], v[136:137], v[146:147] op_sel_hi:[1,0]
	v_pk_mul_f32 v[138:139], v[138:139], v[146:147] op_sel_hi:[1,0]
	v_pk_mul_f32 v[86:87], v[86:87], v[146:147] op_sel_hi:[1,0]
	v_pk_mul_f32 v[142:143], v[142:143], v[146:147] op_sel_hi:[1,0]
	v_pk_mul_f32 v[90:91], v[90:91], v[146:147] op_sel_hi:[1,0]
	v_pk_mul_f32 v[104:105], v[104:105], v[146:147] op_sel_hi:[1,0]
	v_pk_mul_f32 v[148:149], v[108:109], v[146:147] op_sel_hi:[1,0]
	v_pk_mul_f32 v[146:147], v[110:111], v[146:147] op_sel_hi:[1,0]
	v_pk_fma_f32 v[108:109], v[28:29], v[112:113], v[60:61]
	v_pk_fma_f32 v[110:111], v[26:27], v[116:117], v[12:13]
	v_pk_fma_f32 v[12:13], v[32:33], v[120:121], v[62:63]
	v_pk_fma_f32 v[14:15], v[30:31], v[122:123], v[14:15]
	v_pk_fma_f32 v[62:63], v[34:35], v[128:129], v[8:9]
	v_pk_fma_f32 v[8:9], v[40:41], v[130:131], v[144:145]
	v_pk_fma_f32 v[10:11], v[38:39], v[134:135], v[10:11]
	v_pk_fma_f32 v[122:123], v[42:43], v[138:139], v[4:5]
	v_pk_fma_f32 v[4:5], v[48:49], v[86:87], v[198:199]
	v_pk_fma_f32 v[6:7], v[46:47], v[142:143], v[6:7]
	v_pk_fma_f32 v[128:129], v[50:51], v[104:105], v[0:1]
	v_pk_fma_f32 v[0:1], v[56:57], v[148:149], v[202:203]
	v_pk_fma_f32 v[2:3], v[54:55], v[146:147], v[2:3]
	v_pk_fma_f32 v[60:61], v[36:37], v[126:127], v[80:81]
	v_pk_fma_f32 v[120:121], v[44:45], v[136:137], v[190:191]
	v_pk_fma_f32 v[126:127], v[52:53], v[90:91], v[200:201]
	global_store_dwordx4 v[58:59], v[108:111], off offset:-4096
	global_store_dwordx4 v[58:59], v[12:15], off offset:-4080
	global_store_dwordx4 v[58:59], v[60:63], off offset:-2048
	global_store_dwordx4 v[58:59], v[8:11], off offset:-2032
	global_store_dwordx4 v[58:59], v[120:123], off
	global_store_dwordx4 v[58:59], v[4:7], off offset:16
	global_store_dwordx4 v[58:59], v[126:129], off offset:2048
	global_store_dwordx4 v[58:59], v[0:3], off offset:2064
	s_waitcnt vmcnt(9)
	v_mov_b64_e32 v[4:5], v[94:95]
	v_mov_b64_e32 v[8:9], v[82:83]
	s_waitcnt vmcnt(8)
	v_mov_b64_e32 v[0:1], v[100:101]
	v_mov_b64_e32 v[12:13], v[74:75]
	v_lshl_add_u64 v[58:59], v[58:59], 0, s[6:7]
	v_mov_b64_e32 v[2:3], v[102:103]
	v_mov_b64_e32 v[6:7], v[96:97]
	v_mov_b64_e32 v[10:11], v[84:85]
	v_mov_b64_e32 v[14:15], v[76:77]
	s_cbranch_vccnz .LBB0_1344
